# ragged MoE tiles also skip the all-padding second row half MFMAs in the down-projection GEMM (P8)
# speedup vs baseline: 1.0071x; 1.0015x over previous
.LBB0_1146:
	s_add_u32 s10, s90, 0x100000
	s_addc_u32 s11, s91, 0
	v_and_b32_e32 v1, 15, v0
	s_add_u32 s12, s90, 0x29100000
	v_or_b32_e32 v2, s0, v1
	s_addc_u32 s13, s91, 0
	v_lshlrev_b32_e32 v4, 6, v2
	v_and_b32_e32 v5, 48, v0
	s_movk_i32 s4, 0x3c0
	v_and_or_b32 v4, v4, s4, v5
	s_add_u32 s4, s36, 0x80
	s_waitcnt vmcnt(2)
	s_barrier
	s_addc_u32 s5, s37, 0
	s_add_i32 s54, s2, 0x18000
	s_mov_b32 s14, m0
	s_mov_b32 m0, s54
	s_nop 2
	global_load_lds_dwordx4 v162, s[4:5]
	s_mov_b32 m0, s14
	s_add_i32 s55, s2, 0x1a000
	s_mov_b32 s14, m0
	s_mov_b32 m0, s55
	s_nop 2
	global_load_lds_dwordx4 v163, s[4:5]
	s_mov_b32 m0, s14
	s_add_u32 s4, s34, 0x80
	s_addc_u32 s5, s35, 0
	s_add_i32 s62, s2, 0x8000
	s_mov_b32 s14, m0
	s_mov_b32 m0, s62
	s_nop 2
	global_load_lds_dwordx4 v164, s[4:5]
	s_mov_b32 m0, s14
	s_add_i32 s63, s2, 0xa000
	s_mov_b32 s14, m0
	s_mov_b32 m0, s63
	s_nop 2
	global_load_lds_dwordx4 v165, s[4:5]
	s_mov_b32 m0, s14
	s_add_u32 s4, s46, 0x80
	v_ashrrev_i32_e32 v3, 6, v0
	v_lshlrev_b32_e32 v0, 2, v0
	s_addc_u32 s5, s47, 0
	s_add_i32 s64, s2, 0x1c000
	s_mov_b32 s14, m0
	s_mov_b32 m0, s64
	s_nop 2
	global_load_lds_dwordx4 v162, s[4:5]
	s_mov_b32 m0, s14
	v_lshl_add_u32 v6, v3, 10, s33
	v_lshlrev_b32_e32 v2, 2, v2
	v_lshl_or_b32 v1, v1, 6, v5
	v_add_lshl_u32 v3, v3, s38, 10
	v_and_b32_e32 v0, 32, v0
	s_add_i32 s65, s2, 0x1e000
	s_mov_b32 s14, m0
	s_mov_b32 m0, s65
	s_nop 2
	global_load_lds_dwordx4 v163, s[4:5]
	s_mov_b32 m0, s14
	v_and_b32_e32 v2, 32, v2
	v_bitop3_b32 v0, v1, v3, v0 bitop3:0xde
	s_waitcnt vmcnt(6)
	s_add_i32 s66, s2, 0xc000
	v_readlane_b32 s4, v255, 0
	v_bitop3_b32 v2, v4, v6, v2 bitop3:0xde
	s_cmpk_lt_u32 s4, 0x100
	v_add_u32_e32 v0, 0, v0
	s_cselect_b64 s[14:15], -1, 0
	s_add_i32 s67, s2, 0xe000
	v_add_u32_e32 v166, 0x10000, v0
	v_add_u32_e32 v167, 0x14000, v0
	v_add_u32_e32 v168, 0, v2
	v_mov_b32_e32 v169, 0x7f7f7f7f
	v_add_u32_e32 v170, 0x18000, v0
	v_add_u32_e32 v171, 0x1c000, v0
	s_mov_b32 s16, 0x3b000000
	s_mov_b32 s18, 0x41800000
	s_barrier
	v_readlane_b32 s32, v255, 28
	s_lshr_b32 s32, s32, 2
	s_lshl_b32 s32, s32, 6
	s_addk_i32 s32, 0x80
	s_branch .LBB0_1149

.LBB0_1153:
	ds_read_b128 v[128:131], v166
	ds_read_b128 v[132:135], v166 offset:1024
	ds_read_b128 v[136:139], v166 offset:2048
	ds_read_b128 v[140:143], v166 offset:3072
	s_waitcnt vmcnt(0)
	ds_read_b128 v[144:147], v167
	ds_read_b128 v[148:151], v167 offset:1024
	ds_read_b128 v[152:155], v167 offset:2048
	ds_read_b128 v[156:159], v167 offset:3072
	s_add_u32 s36, s34, 0x100
	s_addc_u32 s37, s35, 0
	s_cmp_eq_u32 s80, 12
	s_cselect_b32 s60, s73, s76
	s_cselect_b32 s61, s72, s77
	s_cselect_b32 s47, s74, s79
	s_cselect_b32 s46, s75, s78
	s_cselect_b32 s58, s29, s36
	s_cselect_b32 s59, s5, s37
	s_add_u32 s56, s60, 0x80
	s_addc_u32 s57, s61, 0
	s_add_u32 s50, s58, 0x80
	s_addc_u32 s51, s59, 0
	ds_read_b128 v[172:175], v168
	ds_read_b128 v[176:179], v168 offset:1024
	ds_read_b128 v[180:183], v168 offset:2048
	ds_read_b128 v[184:187], v168 offset:3072
	ds_read_b128 v[188:191], v168 offset:4096
	ds_read_b128 v[192:195], v168 offset:5120
	ds_read_b128 v[196:199], v168 offset:6144
	ds_read_b128 v[200:203], v168 offset:7168
	s_add_u32 s34, s34, 0x40080
	s_addc_u32 s35, s35, 0
	s_mov_b32 s81, m0
	s_mov_b32 m0, s66
	s_nop 2
	global_load_lds_dwordx4 v164, s[34:35]
	s_mov_b32 m0, s81
	s_nop 0
	s_mov_b32 s81, m0
	s_mov_b32 m0, s67
	s_nop 2
	global_load_lds_dwordx4 v165, s[34:35]
	s_mov_b32 m0, s81
	s_waitcnt vmcnt(8)
	s_waitcnt lgkmcnt(0)
	s_barrier
	s_setprio 1
	s_waitcnt lgkmcnt(6)
	v_mfma_scale_f32_16x16x128_f8f6f4 v[124:127], v[128:135], v[172:179], v[124:127], v169, v169 op_sel_hi:[0,0,0]
	v_mfma_scale_f32_16x16x128_f8f6f4 v[120:123], v[136:143], v[172:179], v[120:123], v169, v169 op_sel_hi:[0,0,0]
	s_waitcnt lgkmcnt(4)
	v_mfma_scale_f32_16x16x128_f8f6f4 v[108:111], v[128:135], v[180:187], v[108:111], v169, v169 op_sel_hi:[0,0,0]
	v_mfma_scale_f32_16x16x128_f8f6f4 v[104:107], v[136:143], v[180:187], v[104:107], v169, v169 op_sel_hi:[0,0,0]
	s_waitcnt lgkmcnt(2)
	v_mfma_scale_f32_16x16x128_f8f6f4 v[204:207], v[128:135], v[188:195], v[92:95], v169, v169 op_sel_hi:[0,0,0]
	v_mfma_scale_f32_16x16x128_f8f6f4 v[208:211], v[136:143], v[188:195], v[88:91], v169, v169 op_sel_hi:[0,0,0]
	s_waitcnt lgkmcnt(0)
	v_mfma_scale_f32_16x16x128_f8f6f4 v[212:215], v[128:135], v[196:203], v[76:79], v169, v169 op_sel_hi:[0,0,0]
	v_mfma_scale_f32_16x16x128_f8f6f4 v[216:219], v[136:143], v[196:203], v[72:75], v169, v169 op_sel_hi:[0,0,0]
	s_setprio 0
	s_setprio 1
	v_mfma_scale_f32_16x16x128_f8f6f4 v[116:119], v[144:151], v[172:179], v[116:119], v169, v169 op_sel_hi:[0,0,0]
	v_mfma_scale_f32_16x16x128_f8f6f4 v[112:115], v[152:159], v[172:179], v[112:115], v169, v169 op_sel_hi:[0,0,0]
	v_mfma_scale_f32_16x16x128_f8f6f4 v[100:103], v[144:151], v[180:187], v[100:103], v169, v169 op_sel_hi:[0,0,0]
	v_mfma_scale_f32_16x16x128_f8f6f4 v[96:99], v[152:159], v[180:187], v[96:99], v169, v169 op_sel_hi:[0,0,0]
	v_mfma_scale_f32_16x16x128_f8f6f4 v[172:175], v[144:151], v[188:195], v[84:87], v169, v169 op_sel_hi:[0,0,0]
	v_mfma_scale_f32_16x16x128_f8f6f4 v[176:179], v[152:159], v[188:195], v[80:83], v169, v169 op_sel_hi:[0,0,0]
	v_mfma_scale_f32_16x16x128_f8f6f4 v[180:183], v[144:151], v[196:203], v[68:71], v169, v169 op_sel_hi:[0,0,0]
	v_mfma_scale_f32_16x16x128_f8f6f4 v[184:187], v[152:159], v[196:203], v[64:67], v169, v169 op_sel_hi:[0,0,0]
	s_setprio 0
	s_barrier
	s_nop 4
	ds_read_b128 v[64:67], v168 offset:16384
	ds_read_b128 v[68:71], v168 offset:17408
	ds_read_b128 v[72:75], v168 offset:18432
	ds_read_b128 v[76:79], v168 offset:19456
	ds_read_b128 v[80:83], v168 offset:20480
	ds_read_b128 v[84:87], v168 offset:21504
	ds_read_b128 v[88:91], v168 offset:22528
	ds_read_b128 v[92:95], v168 offset:23552
	s_mov_b32 s34, m0
	s_mov_b32 m0, s31
	s_nop 2
	global_load_lds_dwordx4 v162, s[60:61]
	s_mov_b32 m0, s34
	s_nop 0
	s_mov_b32 s34, m0
	s_mov_b32 m0, s44
	s_nop 2
	global_load_lds_dwordx4 v163, s[60:61]
	s_mov_b32 m0, s34
	s_nop 0
	s_mov_b32 s34, m0
	s_mov_b32 m0, s45
	s_nop 2
	global_load_lds_dwordx4 v162, s[46:47]
	s_mov_b32 m0, s34
	s_nop 0
	s_mov_b32 s34, m0
	s_mov_b32 m0, s48
	s_nop 2
	global_load_lds_dwordx4 v163, s[46:47]
	s_mov_b32 m0, s34
	s_nop 0
	s_mov_b32 s34, m0
	s_mov_b32 m0, s2
	s_nop 2
	global_load_lds_dwordx4 v164, s[58:59]
	s_mov_b32 m0, s34
	s_nop 0
	s_mov_b32 s34, m0
	s_mov_b32 m0, s49
	s_nop 2
	global_load_lds_dwordx4 v165, s[58:59]
	s_mov_b32 m0, s34
	s_waitcnt vmcnt(8)
	s_waitcnt lgkmcnt(0)
	s_barrier
	s_cmp_le_i32 s42, s32
	s_cbranch_scc1 .Lp8_rag_1
	s_setprio 1
	s_waitcnt lgkmcnt(6)
	v_mfma_scale_f32_16x16x128_f8f6f4 v[60:63], v[128:135], v[64:71], v[60:63], v169, v169 op_sel_hi:[0,0,0]
	v_mfma_scale_f32_16x16x128_f8f6f4 v[56:59], v[136:143], v[64:71], v[56:59], v169, v169 op_sel_hi:[0,0,0]
	s_waitcnt lgkmcnt(4)
	v_mfma_scale_f32_16x16x128_f8f6f4 v[188:191], v[128:135], v[72:79], v[44:47], v169, v169 op_sel_hi:[0,0,0]
	v_mfma_scale_f32_16x16x128_f8f6f4 v[192:195], v[136:143], v[72:79], v[40:43], v169, v169 op_sel_hi:[0,0,0]
	s_waitcnt lgkmcnt(2)
	v_mfma_scale_f32_16x16x128_f8f6f4 v[196:199], v[128:135], v[80:87], v[24:27], v169, v169 op_sel_hi:[0,0,0]
	v_mfma_scale_f32_16x16x128_f8f6f4 v[200:203], v[136:143], v[80:87], v[12:15], v169, v169 op_sel_hi:[0,0,0]
	s_waitcnt lgkmcnt(0)
	v_mfma_scale_f32_16x16x128_f8f6f4 v[220:223], v[128:135], v[88:95], v[4:7], v169, v169 op_sel_hi:[0,0,0]
	v_mfma_scale_f32_16x16x128_f8f6f4 v[224:227], v[136:143], v[88:95], v[0:3], v169, v169 op_sel_hi:[0,0,0]
	s_setprio 0
	s_setprio 1
	v_mfma_scale_f32_16x16x128_f8f6f4 v[52:55], v[144:151], v[64:71], v[52:55], v169, v169 op_sel_hi:[0,0,0]
	v_mfma_scale_f32_16x16x128_f8f6f4 v[48:51], v[152:159], v[64:71], v[48:51], v169, v169 op_sel_hi:[0,0,0]
	v_mfma_scale_f32_16x16x128_f8f6f4 v[228:231], v[144:151], v[72:79], v[28:31], v169, v169 op_sel_hi:[0,0,0]
	v_mfma_scale_f32_16x16x128_f8f6f4 v[232:235], v[152:159], v[72:79], v[20:23], v169, v169 op_sel_hi:[0,0,0]
	v_mfma_scale_f32_16x16x128_f8f6f4 v[236:239], v[144:151], v[80:87], v[36:39], v169, v169 op_sel_hi:[0,0,0]
	v_mfma_scale_f32_16x16x128_f8f6f4 v[240:243], v[152:159], v[80:87], v[32:35], v169, v169 op_sel_hi:[0,0,0]
	v_mfma_scale_f32_16x16x128_f8f6f4 v[244:247], v[144:151], v[88:95], v[16:19], v169, v169 op_sel_hi:[0,0,0]
	v_mfma_scale_f32_16x16x128_f8f6f4 v[248:251], v[152:159], v[88:95], v[8:11], v169, v169 op_sel_hi:[0,0,0]
	s_setprio 0
.Lp8_rag_1:
	s_barrier
	ds_read_b128 v[0:3], v170
	ds_read_b128 v[4:7], v170 offset:1024
	s_nop 1
	ds_read_b128 v[16:19], v170 offset:2048
	ds_read_b128 v[20:23], v170 offset:3072
	ds_read_b128 v[128:131], v171
	ds_read_b128 v[132:135], v171 offset:1024
	ds_read_b128 v[136:139], v171 offset:2048
	ds_read_b128 v[140:143], v171 offset:3072
	ds_read_b128 v[8:11], v168 offset:32768
	ds_read_b128 v[12:15], v168 offset:33792
	ds_read_b128 v[24:27], v168 offset:34816
	ds_read_b128 v[28:31], v168 offset:35840
	ds_read_b128 v[32:35], v168 offset:36864
	ds_read_b128 v[36:39], v168 offset:37888
	ds_read_b128 v[40:43], v168 offset:38912
	ds_read_b128 v[44:47], v168 offset:39936
	s_add_u32 s34, s58, 0x40000
	s_addc_u32 s35, s59, 0
	s_mov_b32 s58, m0
	s_mov_b32 m0, s52
	s_nop 2
	global_load_lds_dwordx4 v164, s[34:35]
	s_mov_b32 m0, s58
	s_nop 0
	s_mov_b32 s58, m0
	s_mov_b32 m0, s53
	s_nop 2
	global_load_lds_dwordx4 v165, s[34:35]
	s_mov_b32 m0, s58
	s_waitcnt vmcnt(8)
	s_waitcnt lgkmcnt(0)
	s_barrier
	s_setprio 1
	s_waitcnt lgkmcnt(6)
	v_mfma_scale_f32_16x16x128_f8f6f4 v[124:127], v[0:7], v[8:15], v[124:127], v169, v169 op_sel_hi:[0,0,0]
	v_mfma_scale_f32_16x16x128_f8f6f4 v[120:123], v[16:23], v[8:15], v[120:123], v169, v169 op_sel_hi:[0,0,0]
	s_waitcnt lgkmcnt(4)
	v_mfma_scale_f32_16x16x128_f8f6f4 v[108:111], v[0:7], v[24:31], v[108:111], v169, v169 op_sel_hi:[0,0,0]
	v_mfma_scale_f32_16x16x128_f8f6f4 v[104:107], v[16:23], v[24:31], v[104:107], v169, v169 op_sel_hi:[0,0,0]
	s_waitcnt lgkmcnt(2)
	v_mfma_scale_f32_16x16x128_f8f6f4 v[92:95], v[0:7], v[32:39], v[204:207], v169, v169 op_sel_hi:[0,0,0]
	v_mfma_scale_f32_16x16x128_f8f6f4 v[88:91], v[16:23], v[32:39], v[208:211], v169, v169 op_sel_hi:[0,0,0]
	s_waitcnt lgkmcnt(0)
	v_mfma_scale_f32_16x16x128_f8f6f4 v[76:79], v[0:7], v[40:47], v[212:215], v169, v169 op_sel_hi:[0,0,0]
	v_mfma_scale_f32_16x16x128_f8f6f4 v[72:75], v[16:23], v[40:47], v[216:219], v169, v169 op_sel_hi:[0,0,0]
	s_setprio 0
	s_setprio 1
	v_mfma_scale_f32_16x16x128_f8f6f4 v[116:119], v[128:135], v[8:15], v[116:119], v169, v169 op_sel_hi:[0,0,0]
	v_mfma_scale_f32_16x16x128_f8f6f4 v[112:115], v[136:143], v[8:15], v[112:115], v169, v169 op_sel_hi:[0,0,0]
	v_mfma_scale_f32_16x16x128_f8f6f4 v[100:103], v[128:135], v[24:31], v[100:103], v169, v169 op_sel_hi:[0,0,0]
	v_mfma_scale_f32_16x16x128_f8f6f4 v[96:99], v[136:143], v[24:31], v[96:99], v169, v169 op_sel_hi:[0,0,0]
	v_mfma_scale_f32_16x16x128_f8f6f4 v[84:87], v[128:135], v[32:39], v[172:175], v169, v169 op_sel_hi:[0,0,0]
	v_mfma_scale_f32_16x16x128_f8f6f4 v[80:83], v[136:143], v[32:39], v[176:179], v169, v169 op_sel_hi:[0,0,0]
	v_mfma_scale_f32_16x16x128_f8f6f4 v[68:71], v[128:135], v[40:47], v[180:183], v169, v169 op_sel_hi:[0,0,0]
	v_mfma_scale_f32_16x16x128_f8f6f4 v[64:67], v[136:143], v[40:47], v[184:187], v169, v169 op_sel_hi:[0,0,0]
	s_setprio 0
	s_barrier
	ds_read_b128 v[28:31], v168 offset:49152
	ds_read_b128 v[32:35], v168 offset:50176
	ds_read_b128 v[144:147], v168 offset:51200
	ds_read_b128 v[148:151], v168 offset:52224
	ds_read_b128 v[152:155], v168 offset:53248
	ds_read_b128 v[156:159], v168 offset:54272
	ds_read_b128 v[172:175], v168 offset:55296
	ds_read_b128 v[176:179], v168 offset:56320
	s_mov_b32 s34, m0
	s_mov_b32 m0, s54
	s_nop 2
	global_load_lds_dwordx4 v162, s[56:57]
	s_mov_b32 m0, s34
	s_nop 0
	s_mov_b32 s34, m0
	s_mov_b32 m0, s55
	s_nop 2
	global_load_lds_dwordx4 v163, s[56:57]
	s_mov_b32 m0, s34
	s_add_u32 s34, s46, 0x80
	s_addc_u32 s35, s47, 0
	s_mov_b32 s46, m0
	s_mov_b32 m0, s64
	s_nop 2
	global_load_lds_dwordx4 v162, s[34:35]
	s_mov_b32 m0, s46
	s_nop 0
	s_mov_b32 s46, m0
	s_mov_b32 m0, s65
	s_nop 2
	global_load_lds_dwordx4 v163, s[34:35]
	s_mov_b32 m0, s46
	s_mov_b32 s34, m0
	s_mov_b32 m0, s62
	s_nop 2
	global_load_lds_dwordx4 v164, s[50:51]
	s_mov_b32 m0, s34
	s_nop 0
	s_mov_b32 s34, m0
	s_mov_b32 m0, s63
	s_nop 2
	global_load_lds_dwordx4 v165, s[50:51]
	s_mov_b32 m0, s34
	s_waitcnt vmcnt(8)
	s_waitcnt lgkmcnt(0)
	s_barrier
	s_cmp_le_i32 s42, s32
	s_cbranch_scc1 .Lp8_rag_3
	s_setprio 1
	s_waitcnt lgkmcnt(6)
	v_mfma_scale_f32_16x16x128_f8f6f4 v[60:63], v[0:7], v[28:35], v[60:63], v169, v169 op_sel_hi:[0,0,0]
	v_mfma_scale_f32_16x16x128_f8f6f4 v[56:59], v[16:23], v[28:35], v[56:59], v169, v169 op_sel_hi:[0,0,0]
	s_waitcnt lgkmcnt(4)
	v_mfma_scale_f32_16x16x128_f8f6f4 v[44:47], v[0:7], v[144:151], v[188:191], v169, v169 op_sel_hi:[0,0,0]
	v_mfma_scale_f32_16x16x128_f8f6f4 v[40:43], v[16:23], v[144:151], v[192:195], v169, v169 op_sel_hi:[0,0,0]
	s_waitcnt lgkmcnt(2)
	v_mfma_scale_f32_16x16x128_f8f6f4 v[24:27], v[0:7], v[152:159], v[196:199], v169, v169 op_sel_hi:[0,0,0]
	v_mfma_scale_f32_16x16x128_f8f6f4 v[12:15], v[16:23], v[152:159], v[200:203], v169, v169 op_sel_hi:[0,0,0]
	s_waitcnt lgkmcnt(0)
	v_mfma_scale_f32_16x16x128_f8f6f4 v[4:7], v[0:7], v[172:179], v[220:223], v169, v169 op_sel_hi:[0,0,0]
	v_mfma_scale_f32_16x16x128_f8f6f4 v[0:3], v[16:23], v[172:179], v[224:227], v169, v169 op_sel_hi:[0,0,0]
	s_setprio 0
	s_setprio 1
	v_mfma_scale_f32_16x16x128_f8f6f4 v[52:55], v[128:135], v[28:35], v[52:55], v169, v169 op_sel_hi:[0,0,0]
	v_mfma_scale_f32_16x16x128_f8f6f4 v[48:51], v[136:143], v[28:35], v[48:51], v169, v169 op_sel_hi:[0,0,0]
	v_mfma_scale_f32_16x16x128_f8f6f4 v[28:31], v[128:135], v[144:151], v[228:231], v169, v169 op_sel_hi:[0,0,0]
	v_mfma_scale_f32_16x16x128_f8f6f4 v[20:23], v[136:143], v[144:151], v[232:235], v169, v169 op_sel_hi:[0,0,0]
	v_mfma_scale_f32_16x16x128_f8f6f4 v[36:39], v[128:135], v[152:159], v[236:239], v169, v169 op_sel_hi:[0,0,0]
	v_mfma_scale_f32_16x16x128_f8f6f4 v[32:35], v[136:143], v[152:159], v[240:243], v169, v169 op_sel_hi:[0,0,0]
	v_mfma_scale_f32_16x16x128_f8f6f4 v[16:19], v[128:135], v[172:179], v[244:247], v169, v169 op_sel_hi:[0,0,0]
	v_mfma_scale_f32_16x16x128_f8f6f4 v[8:11], v[136:143], v[172:179], v[248:251], v169, v169 op_sel_hi:[0,0,0]
	s_setprio 0
.Lp8_rag_3:
	s_barrier
	s_add_i32 s80, s80, 2
	s_add_u32 s76, s76, 0x100
	s_addc_u32 s77, s77, 0
	s_add_u32 s78, s78, 0x100
	s_addc_u32 s79, s79, 0
	s_cmp_gt_u32 s80, 13
	s_mov_b64 s[34:35], s[36:37]
	s_cbranch_scc0 .LBB0_1153
	s_and_b64 vcc, exec, s[14:15]
	s_cbranch_vccz .LBB0_1156
	s_barrier
